# attention task prologue: bias-table load, clip-pad scalar load and q/K/V loads issued together before the LDS table writes (one exposed latency instead of three)
# speedup vs baseline: 1.0296x; 1.0003x over previous
; #define GAS __attribute__((address_space(1)))
; #define AT_STAGE_LOAD(kc_) do { kreg = *(const GAS v4u*)(PROJ + ((size_t)b * SEQ + (size_t)(kc_) * 64 + srow) * PROJ_LD + PJ_K + h * 64 + spc * 8); \
;                                 vreg = *(const GAS v4u*)(VT + (size_t)(h * 64 + srow) * T + (size_t)b * SEQ + (size_t)(kc_) * 64 + spc * 8); } while (0)
; #define AT_STAGE_WRITE(buf_) do { *(LAS v4u*)(F.lds + A_KOFF + (buf_) * AKV + srow * 144 + spc * 16) = kreg; *(LAS v4u*)(F.lds + A_VOFF + (buf_) * AKV + srow * 144 + spc * 16) = vreg; } while (0)
; __device__ __forceinline__ void p2_shift_attn(Frame& F0, const In& I) {
;     ...
;     for (int task = F.vcu; task < BATCH * AH * (SEQ / 256); task += F.G) {
;         const int bh = task >> 5, q256 = task & 31, b = bh >> 4, h = bh & 15, c0 = q256 * 4;
;         const int q0 = q256 * 256 + F.wave * 32, cw = c0 + (F.wave >> 1);
;         const int kc_lo = (c0 > LEFT) ? c0 - LEFT : 0, kc_hi = c0 + 3;
;         __syncthreads();
;         if (F.tid < REL_TABLE) tbl[F.tid] = I.rel_bias[h * REL_TABLE + F.tid];
;         const size_t tokq = (size_t)b * SEQ + q0 + r;
;         bf16x8 qf[4];
; #pragma unroll
;         for (int s = 0; s < 4; ++s) qf[s] = *(const GAS bf16x8*)(PROJ + tokq * PROJ_LD + PJ_Q + h * 64 + 16 * s + 8 * hh);
;         f32x16 o0, o1;
; #pragma unroll
;         for (int i = 0; i < 16; ++i) { o0[i] = 0.f; o1[i] = 0.f; }
;         float m_run = -1e30f, l_run = 0.f;
;         v4u kreg, vreg;
;     ...
;         AT_STAGE_LOAD(kc_lo); AT_STAGE_WRITE(0);
;         __syncthreads();
.LBB0_878:
	s_or_b64 exec, exec, s[12:13]
	v_readlane_b32 s100, v254, 9
	v_readlane_b32 s101, v254, 10
	s_mul_i32 s98, s16, 0x140
	s_add_i32 s98, s98, 319
	s_lshl_b32 s98, s98, 2
	s_nop 4
	s_load_dword s99, s[100:101], s98
	s_and_b32 s8, s26, 31
	s_lshl_b32 s28, s8, 2
	s_lshl_b32 s12, s8, 8
	s_ashr_i32 s14, s26, 9
	s_add_i32 s13, s12, s20
	s_add_i32 s12, s28, -8
	s_cmp_gt_u32 s8, 2
	s_cselect_b32 s12, s12, 0
	s_ashr_i32 s15, s14, 31
	s_or_b32 s27, s28, 3
	s_lshl_b64 s[18:19], s[14:15], 13
	s_ashr_i32 s8, s13, 31
	s_add_u32 s13, s18, s13
	v_or_b32_e32 v140, s13, v124
	s_addc_u32 s29, s19, s8
	v_mad_u64_u32 v[4:5], s[30:31], v140, s23, v[134:135]
	s_ashr_i32 s13, s12, 31
	s_lshl_b32 s8, s16, 6
	s_lshl_b32 s16, s16, 7
	s_lshl_b64 s[30:31], s[12:13], 6
	s_add_u32 s18, s30, s18
	s_addc_u32 s19, s31, s19
	v_lshl_add_u64 v[6:7], s[18:19], 0, v[126:127]
	v_mad_u64_u32 v[8:9], s[18:19], v6, s23, v[134:135]
	s_mov_b32 s17, s9
	v_mad_i32_i24 v9, v7, s23, v9
	v_lshl_add_u64 v[6:7], v[8:9], 0, s[16:17]
	v_add_u32_e32 v8, s8, v126
	v_ashrrev_i32_e32 v9, 31, v8
	v_mad_i32_i24 v5, s29, v167, v5
	v_lshlrev_b64 v[8:9], 16, v[8:9]
	v_lshl_add_u64 v[4:5], v[4:5], 0, s[16:17]
	v_lshl_add_u64 v[8:9], s[0:1], 0, v[8:9]
	s_lshl_b64 s[16:17], s[14:15], 14
	v_lshl_add_u64 v[8:9], v[8:9], 0, s[16:17]
	s_lshl_b64 s[18:19], s[12:13], 7
	v_lshl_add_u64 v[6:7], v[6:7], 0, v[138:139]
	v_lshl_add_u64 v[8:9], v[8:9], 0, s[18:19]
	v_lshl_add_u64 v[4:5], v[4:5], 0, v[136:137]
	v_lshl_add_u64 v[8:9], v[8:9], 0, v[138:139]
	global_load_dwordx4 v[68:71], v[6:7], off offset:2048
	global_load_dwordx4 v[80:83], v[8:9], off
	global_load_dwordx4 v[72:75], v[4:5], off
	global_load_dwordx4 v[76:79], v[4:5], off offset:32
	global_load_dwordx4 v[84:87], v[4:5], off offset:64
	global_load_dwordx4 v[88:91], v[4:5], off offset:96
	v_mov_b32_e32 v141, s29
	s_waitcnt vmcnt(6)
	s_mov_b64 s[100:101], exec
	s_and_b64 exec, exec, s[2:3]
	ds_write_b32 v125, v3
	ds_write_b32 v125, v3 offset:40960
	s_mov_b64 exec, s[100:101]
	s_waitcnt lgkmcnt(0)
	v_mov_b32_e32 v177, s99
	ds_write_b32 v125, v177 offset:42240
	s_cmp_gt_i32 s12, s27
	s_waitcnt vmcnt(5)
	ds_write_b128 v162, v[68:71] offset:2048
	s_waitcnt vmcnt(4)
	ds_write_b128 v162, v[80:83] offset:20480
	s_waitcnt vmcnt(0) lgkmcnt(0)
	s_barrier
	s_cbranch_scc1 .LBB0_874
	s_lshr_b32 s13, s26, 5
	s_and_b32 s15, s25, 31
	s_lshl_b32 s15, s15, 8
	s_and_b32 s13, s13, 15
	v_lshl_add_u32 v4, s13, 6, v126
	s_lshl_b32 s30, s13, 7
	s_add_i32 s13, s28, s21
	s_add_i32 s15, s22, s15
	s_lshl_b32 s29, s12, 6
	s_add_i32 s28, s13, -8
	s_sub_i32 s29, s15, s29
	v_ashrrev_i32_e32 v5, 31, v4
	s_add_u32 s16, s18, s16
	v_lshlrev_b64 v[4:5], 16, v[4:5]
	s_addc_u32 s17, s19, s17
	v_lshl_add_u64 v[4:5], s[16:17], 0, v[4:5]
	s_mul_hi_i32 s15, s14, 0x2100000
	s_mul_i32 s14, s14, 0x2100000
	s_mul_i32 s17, s12, 0x42000
	v_mov_b32_e32 v16, v2
	v_mov_b32_e32 v17, v2
	v_lshl_add_u64 v[142:143], v[130:131], 0, v[4:5]
	s_mul_hi_i32 s16, s12, 0x42000
	s_add_u32 s14, s14, s17
	v_mov_b32_e32 v3, v2
	v_mov_b32_e32 v4, v2
	v_mov_b32_e32 v5, v2
	v_mov_b32_e32 v6, v2
	v_mov_b32_e32 v7, v2
	v_mov_b32_e32 v8, v2
	v_mov_b32_e32 v9, v2
	v_mov_b32_e32 v10, v2
	v_mov_b32_e32 v11, v2
	v_mov_b32_e32 v12, v2
	v_mov_b32_e32 v13, v2
	v_mov_b32_e32 v14, v2
	v_mov_b32_e32 v15, v2
	v_mov_b64_e32 v[34:35], v[16:17]
	s_addc_u32 s15, s15, s16
	s_or_b32 s14, s14, s30
	v_mov_b64_e32 v[32:33], v[14:15]
	v_mov_b64_e32 v[30:31], v[12:13]
	v_mov_b64_e32 v[28:29], v[10:11]
	v_mov_b64_e32 v[26:27], v[8:9]
	v_mov_b64_e32 v[24:25], v[6:7]
	v_mov_b64_e32 v[22:23], v[4:5]
	v_mov_b64_e32 v[20:21], v[2:3]
	v_mov_b64_e32 v[18:19], v[16:17]
	v_lshl_add_u64 v[144:145], v[132:133], 0, s[14:15]
	v_mov_b32_e32 v168, 0
	v_mov_b32_e32 v169, 0xf149f2ca
	v_mov_b64_e32 v[16:17], v[14:15]
	v_mov_b64_e32 v[14:15], v[12:13]
	v_mov_b64_e32 v[12:13], v[10:11]
	v_mov_b64_e32 v[10:11], v[8:9]
	v_mov_b64_e32 v[8:9], v[6:7]
	v_mov_b64_e32 v[6:7], v[4:5]
	v_mov_b64_e32 v[4:5], v[2:3]
